# speedup vs baseline: 1.0042x; 1.0042x over previous
.Lep1_prej:
	s_waitcnt lgkmcnt(7)
	s_barrier
	s_cmp_eq_u64 s[6:7], 0
	s_cbranch_scc0 .Lep1_k1
	v_mov_b32_e32 v18, 0
	v_mov_b32_e32 v19, 0
	v_mov_b32_e32 v20, 0
	v_mov_b32_e32 v21, 0
	ds_read2st64_b32 v[50:51], v221 offset0:0 offset1:1
	ds_read2st64_b32 v[52:53], v221 offset0:2 offset1:3
	ds_read2st64_b32 v[54:55], v221 offset0:4 offset1:5
	ds_read2st64_b32 v[56:57], v221 offset0:6 offset1:7
	ds_read2st64_b32 v[58:59], v221 offset0:8 offset1:9
	ds_read2st64_b32 v[60:61], v221 offset0:10 offset1:11
	s_waitcnt lgkmcnt(12)
	v_fma_f32 v78, -v76, v77, 0
	s_waitcnt lgkmcnt(4)
	v_pk_add_f32 v[34:35], v[34:35], v[50:51]
	v_pk_add_f32 v[36:37], v[36:37], v[52:53]
	v_pk_add_f32 v[34:35], v[34:35], v[78:79] op_sel_hi:[1,0]
	v_pk_add_f32 v[36:37], v[36:37], v[78:79] op_sel_hi:[1,0]
	v_pk_fma_f32 v[34:35], v[62:63], v[76:77], v[34:35] op_sel:[0,1,0] op_sel_hi:[1,1,1]
	v_pk_fma_f32 v[36:37], v[64:65], v[76:77], v[36:37] op_sel:[0,1,0] op_sel_hi:[1,1,1]
	v_pk_add_f32 v[18:19], v[18:19], v[34:35]
	v_pk_fma_f32 v[20:21], v[34:35], v[34:35], v[20:21]
	v_pk_add_f32 v[18:19], v[18:19], v[36:37]
	v_pk_fma_f32 v[20:21], v[36:37], v[36:37], v[20:21]
	s_waitcnt lgkmcnt(2)
	v_pk_add_f32 v[38:39], v[38:39], v[54:55]
	v_pk_add_f32 v[40:41], v[40:41], v[56:57]
	v_pk_add_f32 v[38:39], v[38:39], v[78:79] op_sel_hi:[1,0]
	v_pk_add_f32 v[40:41], v[40:41], v[78:79] op_sel_hi:[1,0]
	v_pk_fma_f32 v[38:39], v[68:69], v[76:77], v[38:39] op_sel:[0,1,0] op_sel_hi:[1,1,1]
	v_pk_fma_f32 v[40:41], v[70:71], v[76:77], v[40:41] op_sel:[0,1,0] op_sel_hi:[1,1,1]
	v_pk_add_f32 v[18:19], v[18:19], v[38:39]
	v_pk_fma_f32 v[20:21], v[38:39], v[38:39], v[20:21]
	v_pk_add_f32 v[18:19], v[18:19], v[40:41]
	v_pk_fma_f32 v[20:21], v[40:41], v[40:41], v[20:21]
	s_waitcnt lgkmcnt(0)
	v_pk_add_f32 v[42:43], v[42:43], v[58:59]
	v_pk_add_f32 v[44:45], v[44:45], v[60:61]
	v_pk_add_f32 v[42:43], v[42:43], v[78:79] op_sel_hi:[1,0]
	v_pk_add_f32 v[44:45], v[44:45], v[78:79] op_sel_hi:[1,0]
	v_pk_fma_f32 v[42:43], v[72:73], v[76:77], v[42:43] op_sel:[0,1,0] op_sel_hi:[1,1,1]
	v_pk_fma_f32 v[44:45], v[74:75], v[76:77], v[44:45] op_sel:[0,1,0] op_sel_hi:[1,1,1]
	v_pk_add_f32 v[18:19], v[18:19], v[42:43]
	v_pk_fma_f32 v[20:21], v[42:43], v[42:43], v[20:21]
	v_pk_add_f32 v[18:19], v[18:19], v[44:45]
	v_pk_fma_f32 v[20:21], v[44:45], v[44:45], v[20:21]
	ds_read2st64_b32 v[50:51], v221 offset0:12 offset1:13
	ds_read2st64_b32 v[52:53], v221 offset0:14 offset1:15
	ds_read2st64_b32 v[54:55], v221 offset0:16 offset1:17
	ds_read2st64_b32 v[56:57], v221 offset0:18 offset1:19
	ds_read2st64_b32 v[58:59], v221 offset0:20 offset1:21
	ds_read2st64_b32 v[60:61], v221 offset0:22 offset1:23
	ds_read2st64_b32 v[62:63], v67 offset0:48 offset1:50
	ds_read2st64_b32 v[64:65], v67 offset0:52 offset1:54
	ds_read2st64_b32 v[68:69], v67 offset0:64 offset1:66
	ds_read2st64_b32 v[70:71], v67 offset0:68 offset1:70
	ds_read2st64_b32 v[72:73], v67 offset0:80 offset1:82
	ds_read2st64_b32 v[74:75], v67 offset0:84 offset1:86
	s_barrier
	ds_read_b32 v80, v236
	s_waitcnt lgkmcnt(5)
	v_pk_add_f32 v[46:47], v[46:47], v[50:51]
	v_pk_add_f32 v[48:49], v[48:49], v[52:53]
	v_pk_add_f32 v[46:47], v[46:47], v[78:79] op_sel_hi:[1,0]
	v_pk_add_f32 v[48:49], v[48:49], v[78:79] op_sel_hi:[1,0]
	v_pk_fma_f32 v[46:47], v[62:63], v[76:77], v[46:47] op_sel:[0,1,0] op_sel_hi:[1,1,1]
	v_pk_fma_f32 v[48:49], v[64:65], v[76:77], v[48:49] op_sel:[0,1,0] op_sel_hi:[1,1,1]
	v_pk_add_f32 v[18:19], v[18:19], v[46:47]
	v_pk_fma_f32 v[20:21], v[46:47], v[46:47], v[20:21]
	v_pk_add_f32 v[18:19], v[18:19], v[48:49]
	v_pk_fma_f32 v[20:21], v[48:49], v[48:49], v[20:21]
	s_waitcnt lgkmcnt(3)
	v_pk_add_f32 v[2:3], v[2:3], v[54:55]
	v_pk_add_f32 v[4:5], v[4:5], v[56:57]
	v_pk_add_f32 v[2:3], v[2:3], v[78:79] op_sel_hi:[1,0]
	v_pk_add_f32 v[4:5], v[4:5], v[78:79] op_sel_hi:[1,0]
	v_pk_fma_f32 v[2:3], v[68:69], v[76:77], v[2:3] op_sel:[0,1,0] op_sel_hi:[1,1,1]
	v_pk_fma_f32 v[4:5], v[70:71], v[76:77], v[4:5] op_sel:[0,1,0] op_sel_hi:[1,1,1]
	v_pk_add_f32 v[18:19], v[18:19], v[2:3]
	v_pk_fma_f32 v[20:21], v[2:3], v[2:3], v[20:21]
	v_pk_add_f32 v[18:19], v[18:19], v[4:5]
	v_pk_fma_f32 v[20:21], v[4:5], v[4:5], v[20:21]
	s_waitcnt lgkmcnt(1)
	v_pk_add_f32 v[6:7], v[6:7], v[58:59]
	v_pk_add_f32 v[8:9], v[8:9], v[60:61]
	v_pk_add_f32 v[6:7], v[6:7], v[78:79] op_sel_hi:[1,0]
	v_pk_add_f32 v[8:9], v[8:9], v[78:79] op_sel_hi:[1,0]
	v_pk_fma_f32 v[6:7], v[72:73], v[76:77], v[6:7] op_sel:[0,1,0] op_sel_hi:[1,1,1]
	v_pk_fma_f32 v[8:9], v[74:75], v[76:77], v[8:9] op_sel:[0,1,0] op_sel_hi:[1,1,1]
	v_pk_add_f32 v[18:19], v[18:19], v[6:7]
	v_pk_fma_f32 v[20:21], v[6:7], v[6:7], v[20:21]
	v_pk_add_f32 v[18:19], v[18:19], v[8:9]
	v_pk_fma_f32 v[20:21], v[8:9], v[8:9], v[20:21]
	v_add_f32_e32 v18, v18, v19
	v_add_f32_e32 v20, v20, v21
	s_nop 1
	v_permlane32_swap_b32_e32 v18, v20
	v_add_f32_e32 v22, v18, v20
	s_branch .Lep1_wr0
.Lep1_k1:
	s_setprio 2
	v_mov_b32_e32 v34, 0
	v_mov_b32_e32 v35, 0
	v_mov_b32_e32 v36, 0
	v_mov_b32_e32 v37, 0
	ds_read2st64_b32 v[50:51], v221 offset0:24 offset1:25
	ds_read2st64_b32 v[52:53], v221 offset0:26 offset1:27
	ds_read2st64_b32 v[54:55], v221 offset0:28 offset1:29
	ds_read2st64_b32 v[56:57], v221 offset0:30 offset1:31
	ds_read2st64_b32 v[58:59], v221 offset0:32 offset1:33
	ds_read2st64_b32 v[60:61], v221 offset0:34 offset1:35
	s_waitcnt lgkmcnt(12)
	v_fma_f32 v78, -v76, v77, 0
	s_waitcnt lgkmcnt(4)
	v_pk_add_f32 v[10:11], v[10:11], v[50:51]
	v_pk_add_f32 v[12:13], v[12:13], v[52:53]
	v_pk_add_f32 v[10:11], v[10:11], v[78:79] op_sel_hi:[1,0]
	v_pk_add_f32 v[12:13], v[12:13], v[78:79] op_sel_hi:[1,0]
	v_pk_fma_f32 v[10:11], v[62:63], v[76:77], v[10:11] op_sel:[0,1,0] op_sel_hi:[1,1,1]
	v_pk_fma_f32 v[12:13], v[64:65], v[76:77], v[12:13] op_sel:[0,1,0] op_sel_hi:[1,1,1]
	v_pk_add_f32 v[34:35], v[34:35], v[10:11]
	v_pk_fma_f32 v[36:37], v[10:11], v[10:11], v[36:37]
	v_pk_add_f32 v[34:35], v[34:35], v[12:13]
	v_pk_fma_f32 v[36:37], v[12:13], v[12:13], v[36:37]
	s_waitcnt lgkmcnt(2)
	v_pk_add_f32 v[14:15], v[14:15], v[54:55]
	v_pk_add_f32 v[16:17], v[16:17], v[56:57]
	v_pk_add_f32 v[14:15], v[14:15], v[78:79] op_sel_hi:[1,0]
	v_pk_add_f32 v[16:17], v[16:17], v[78:79] op_sel_hi:[1,0]
	v_pk_fma_f32 v[14:15], v[68:69], v[76:77], v[14:15] op_sel:[0,1,0] op_sel_hi:[1,1,1]
	v_pk_fma_f32 v[16:17], v[70:71], v[76:77], v[16:17] op_sel:[0,1,0] op_sel_hi:[1,1,1]
	v_pk_add_f32 v[34:35], v[34:35], v[14:15]
	v_pk_fma_f32 v[36:37], v[14:15], v[14:15], v[36:37]
	v_pk_add_f32 v[34:35], v[34:35], v[16:17]
	v_pk_fma_f32 v[36:37], v[16:17], v[16:17], v[36:37]
	s_waitcnt lgkmcnt(0)
	v_pk_add_f32 v[18:19], v[18:19], v[58:59]
	v_pk_add_f32 v[20:21], v[20:21], v[60:61]
	v_pk_add_f32 v[18:19], v[18:19], v[78:79] op_sel_hi:[1,0]
	v_pk_add_f32 v[20:21], v[20:21], v[78:79] op_sel_hi:[1,0]
	v_pk_fma_f32 v[18:19], v[72:73], v[76:77], v[18:19] op_sel:[0,1,0] op_sel_hi:[1,1,1]
	v_pk_fma_f32 v[20:21], v[74:75], v[76:77], v[20:21] op_sel:[0,1,0] op_sel_hi:[1,1,1]
	v_pk_add_f32 v[34:35], v[34:35], v[18:19]
	v_pk_fma_f32 v[36:37], v[18:19], v[18:19], v[36:37]
	v_pk_add_f32 v[34:35], v[34:35], v[20:21]
	v_pk_fma_f32 v[36:37], v[20:21], v[20:21], v[36:37]
	ds_read2st64_b32 v[50:51], v221 offset0:36 offset1:37
	ds_read2st64_b32 v[52:53], v221 offset0:38 offset1:39
	ds_read2st64_b32 v[62:63], v67 offset0:144 offset1:146
	ds_read2st64_b32 v[64:65], v67 offset0:148 offset1:150
	s_waitcnt lgkmcnt(0)
	v_pk_add_f32 v[22:23], v[22:23], v[50:51]
	v_pk_add_f32 v[24:25], v[24:25], v[52:53]
	v_pk_add_f32 v[22:23], v[22:23], v[78:79] op_sel_hi:[1,0]
	v_pk_add_f32 v[24:25], v[24:25], v[78:79] op_sel_hi:[1,0]
	v_pk_fma_f32 v[22:23], v[62:63], v[76:77], v[22:23] op_sel:[0,1,0] op_sel_hi:[1,1,1]
	v_pk_fma_f32 v[24:25], v[64:65], v[76:77], v[24:25] op_sel:[0,1,0] op_sel_hi:[1,1,1]
	v_pk_add_f32 v[34:35], v[34:35], v[22:23]
	v_pk_fma_f32 v[36:37], v[22:23], v[22:23], v[36:37]
	v_pk_add_f32 v[34:35], v[34:35], v[24:25]
	v_pk_fma_f32 v[36:37], v[24:25], v[24:25], v[36:37]
	s_mov_b64 s[40:41], exec
	s_and_b64 exec, exec, s[0:1]
	ds_read2st64_b32 v[50:51], v221 offset0:40 offset1:41
	ds_read2st64_b32 v[52:53], v221 offset0:42 offset1:43
	ds_read2st64_b32 v[62:63], v67 offset0:160 offset1:162
	ds_read2st64_b32 v[64:65], v67 offset0:164 offset1:166
	s_waitcnt lgkmcnt(0)
	v_pk_add_f32 v[26:27], v[26:27], v[50:51]
	v_pk_add_f32 v[28:29], v[28:29], v[52:53]
	v_pk_add_f32 v[26:27], v[26:27], v[78:79] op_sel_hi:[1,0]
	v_pk_add_f32 v[28:29], v[28:29], v[78:79] op_sel_hi:[1,0]
	v_pk_fma_f32 v[26:27], v[62:63], v[76:77], v[26:27] op_sel:[0,1,0] op_sel_hi:[1,1,1]
	v_pk_fma_f32 v[28:29], v[64:65], v[76:77], v[28:29] op_sel:[0,1,0] op_sel_hi:[1,1,1]
	v_pk_add_f32 v[34:35], v[34:35], v[26:27]
	v_pk_fma_f32 v[36:37], v[26:27], v[26:27], v[36:37]
	v_pk_add_f32 v[34:35], v[34:35], v[28:29]
	v_pk_fma_f32 v[36:37], v[28:29], v[28:29], v[36:37]
	s_mov_b64 exec, s[40:41]
	v_add_f32_e32 v34, v34, v35
	v_add_f32_e32 v36, v36, v37
	s_nop 1
	v_permlane32_swap_b32_e32 v34, v36
	v_add_f32_e32 v38, v34, v36
	ds_write_b32 v236, v38

.Lep2_prej:
	s_waitcnt lgkmcnt(7)
	s_barrier
	s_cmp_eq_u64 s[6:7], 0
	s_cbranch_scc0 .Lep2_k1
	v_mov_b32_e32 v18, 0
	v_mov_b32_e32 v19, 0
	v_mov_b32_e32 v20, 0
	v_mov_b32_e32 v21, 0
	ds_read2st64_b32 v[50:51], v221 offset0:0 offset1:1
	ds_read2st64_b32 v[52:53], v221 offset0:2 offset1:3
	ds_read2st64_b32 v[54:55], v221 offset0:4 offset1:5
	ds_read2st64_b32 v[56:57], v221 offset0:6 offset1:7
	ds_read2st64_b32 v[58:59], v221 offset0:8 offset1:9
	ds_read2st64_b32 v[60:61], v221 offset0:10 offset1:11
	s_waitcnt lgkmcnt(12)
	v_fma_f32 v78, -v76, v77, v173
	s_waitcnt lgkmcnt(4)
	v_pk_add_f32 v[34:35], v[34:35], v[50:51]
	v_pk_add_f32 v[36:37], v[36:37], v[52:53]
	v_pk_add_f32 v[34:35], v[34:35], v[78:79] op_sel_hi:[1,0]
	v_pk_add_f32 v[36:37], v[36:37], v[78:79] op_sel_hi:[1,0]
	v_pk_fma_f32 v[34:35], v[62:63], v[76:77], v[34:35] op_sel:[0,1,0] op_sel_hi:[1,1,1]
	v_pk_fma_f32 v[36:37], v[64:65], v[76:77], v[36:37] op_sel:[0,1,0] op_sel_hi:[1,1,1]
	v_pk_add_f32 v[18:19], v[18:19], v[34:35]
	v_pk_fma_f32 v[20:21], v[34:35], v[34:35], v[20:21]
	v_pk_add_f32 v[18:19], v[18:19], v[36:37]
	v_pk_fma_f32 v[20:21], v[36:37], v[36:37], v[20:21]
	s_waitcnt lgkmcnt(2)
	v_pk_add_f32 v[38:39], v[38:39], v[54:55]
	v_pk_add_f32 v[40:41], v[40:41], v[56:57]
	v_pk_add_f32 v[38:39], v[38:39], v[78:79] op_sel_hi:[1,0]
	v_pk_add_f32 v[40:41], v[40:41], v[78:79] op_sel_hi:[1,0]
	v_pk_fma_f32 v[38:39], v[68:69], v[76:77], v[38:39] op_sel:[0,1,0] op_sel_hi:[1,1,1]
	v_pk_fma_f32 v[40:41], v[70:71], v[76:77], v[40:41] op_sel:[0,1,0] op_sel_hi:[1,1,1]
	v_pk_add_f32 v[18:19], v[18:19], v[38:39]
	v_pk_fma_f32 v[20:21], v[38:39], v[38:39], v[20:21]
	v_pk_add_f32 v[18:19], v[18:19], v[40:41]
	v_pk_fma_f32 v[20:21], v[40:41], v[40:41], v[20:21]
	s_waitcnt lgkmcnt(0)
	v_pk_add_f32 v[42:43], v[42:43], v[58:59]
	v_pk_add_f32 v[44:45], v[44:45], v[60:61]
	v_pk_add_f32 v[42:43], v[42:43], v[78:79] op_sel_hi:[1,0]
	v_pk_add_f32 v[44:45], v[44:45], v[78:79] op_sel_hi:[1,0]
	v_pk_fma_f32 v[42:43], v[72:73], v[76:77], v[42:43] op_sel:[0,1,0] op_sel_hi:[1,1,1]
	v_pk_fma_f32 v[44:45], v[74:75], v[76:77], v[44:45] op_sel:[0,1,0] op_sel_hi:[1,1,1]
	v_pk_add_f32 v[18:19], v[18:19], v[42:43]
	v_pk_fma_f32 v[20:21], v[42:43], v[42:43], v[20:21]
	v_pk_add_f32 v[18:19], v[18:19], v[44:45]
	v_pk_fma_f32 v[20:21], v[44:45], v[44:45], v[20:21]
	ds_read2st64_b32 v[50:51], v221 offset0:12 offset1:13
	ds_read2st64_b32 v[52:53], v221 offset0:14 offset1:15
	ds_read2st64_b32 v[54:55], v221 offset0:16 offset1:17
	ds_read2st64_b32 v[56:57], v221 offset0:18 offset1:19
	ds_read2st64_b32 v[58:59], v221 offset0:20 offset1:21
	ds_read2st64_b32 v[60:61], v221 offset0:22 offset1:23
	ds_read2st64_b32 v[62:63], v67 offset0:48 offset1:50
	ds_read2st64_b32 v[64:65], v67 offset0:52 offset1:54
	ds_read2st64_b32 v[68:69], v67 offset0:64 offset1:66
	ds_read2st64_b32 v[70:71], v67 offset0:68 offset1:70
	ds_read2st64_b32 v[72:73], v67 offset0:80 offset1:82
	ds_read2st64_b32 v[74:75], v67 offset0:84 offset1:86
	s_barrier
	ds_read_b32 v80, v236
	s_waitcnt lgkmcnt(5)
	v_pk_add_f32 v[46:47], v[46:47], v[50:51]
	v_pk_add_f32 v[48:49], v[48:49], v[52:53]
	v_pk_add_f32 v[46:47], v[46:47], v[78:79] op_sel_hi:[1,0]
	v_pk_add_f32 v[48:49], v[48:49], v[78:79] op_sel_hi:[1,0]
	v_pk_fma_f32 v[46:47], v[62:63], v[76:77], v[46:47] op_sel:[0,1,0] op_sel_hi:[1,1,1]
	v_pk_fma_f32 v[48:49], v[64:65], v[76:77], v[48:49] op_sel:[0,1,0] op_sel_hi:[1,1,1]
	v_pk_add_f32 v[18:19], v[18:19], v[46:47]
	v_pk_fma_f32 v[20:21], v[46:47], v[46:47], v[20:21]
	v_pk_add_f32 v[18:19], v[18:19], v[48:49]
	v_pk_fma_f32 v[20:21], v[48:49], v[48:49], v[20:21]
	s_waitcnt lgkmcnt(3)
	v_pk_add_f32 v[2:3], v[2:3], v[54:55]
	v_pk_add_f32 v[4:5], v[4:5], v[56:57]
	v_pk_add_f32 v[2:3], v[2:3], v[78:79] op_sel_hi:[1,0]
	v_pk_add_f32 v[4:5], v[4:5], v[78:79] op_sel_hi:[1,0]
	v_pk_fma_f32 v[2:3], v[68:69], v[76:77], v[2:3] op_sel:[0,1,0] op_sel_hi:[1,1,1]
	v_pk_fma_f32 v[4:5], v[70:71], v[76:77], v[4:5] op_sel:[0,1,0] op_sel_hi:[1,1,1]
	v_pk_add_f32 v[18:19], v[18:19], v[2:3]
	v_pk_fma_f32 v[20:21], v[2:3], v[2:3], v[20:21]
	v_pk_add_f32 v[18:19], v[18:19], v[4:5]
	v_pk_fma_f32 v[20:21], v[4:5], v[4:5], v[20:21]
	s_waitcnt lgkmcnt(1)
	v_pk_add_f32 v[6:7], v[6:7], v[58:59]
	v_pk_add_f32 v[8:9], v[8:9], v[60:61]
	v_pk_add_f32 v[6:7], v[6:7], v[78:79] op_sel_hi:[1,0]
	v_pk_add_f32 v[8:9], v[8:9], v[78:79] op_sel_hi:[1,0]
	v_pk_fma_f32 v[6:7], v[72:73], v[76:77], v[6:7] op_sel:[0,1,0] op_sel_hi:[1,1,1]
	v_pk_fma_f32 v[8:9], v[74:75], v[76:77], v[8:9] op_sel:[0,1,0] op_sel_hi:[1,1,1]
	v_pk_add_f32 v[18:19], v[18:19], v[6:7]
	v_pk_fma_f32 v[20:21], v[6:7], v[6:7], v[20:21]
	v_pk_add_f32 v[18:19], v[18:19], v[8:9]
	v_pk_fma_f32 v[20:21], v[8:9], v[8:9], v[20:21]
	v_add_f32_e32 v18, v18, v19
	v_add_f32_e32 v20, v20, v21
	s_nop 1
	v_permlane32_swap_b32_e32 v18, v20
	v_add_f32_e32 v22, v18, v20
	s_branch .Lep2_wr0
.Lep2_k1:
	s_setprio 2
	v_mov_b32_e32 v34, 0
	v_mov_b32_e32 v35, 0
	v_mov_b32_e32 v36, 0
	v_mov_b32_e32 v37, 0
	ds_read2st64_b32 v[50:51], v221 offset0:24 offset1:25
	ds_read2st64_b32 v[52:53], v221 offset0:26 offset1:27
	ds_read2st64_b32 v[54:55], v221 offset0:28 offset1:29
	ds_read2st64_b32 v[56:57], v221 offset0:30 offset1:31
	ds_read2st64_b32 v[58:59], v221 offset0:32 offset1:33
	ds_read2st64_b32 v[60:61], v221 offset0:34 offset1:35
	s_waitcnt lgkmcnt(12)
	v_fma_f32 v78, -v76, v77, v173
	s_waitcnt lgkmcnt(4)
	v_pk_add_f32 v[10:11], v[10:11], v[50:51]
	v_pk_add_f32 v[12:13], v[12:13], v[52:53]
	v_pk_add_f32 v[10:11], v[10:11], v[78:79] op_sel_hi:[1,0]
	v_pk_add_f32 v[12:13], v[12:13], v[78:79] op_sel_hi:[1,0]
	v_pk_fma_f32 v[10:11], v[62:63], v[76:77], v[10:11] op_sel:[0,1,0] op_sel_hi:[1,1,1]
	v_pk_fma_f32 v[12:13], v[64:65], v[76:77], v[12:13] op_sel:[0,1,0] op_sel_hi:[1,1,1]
	v_pk_add_f32 v[34:35], v[34:35], v[10:11]
	v_pk_fma_f32 v[36:37], v[10:11], v[10:11], v[36:37]
	v_pk_add_f32 v[34:35], v[34:35], v[12:13]
	v_pk_fma_f32 v[36:37], v[12:13], v[12:13], v[36:37]
	s_waitcnt lgkmcnt(2)
	v_pk_add_f32 v[14:15], v[14:15], v[54:55]
	v_pk_add_f32 v[16:17], v[16:17], v[56:57]
	v_pk_add_f32 v[14:15], v[14:15], v[78:79] op_sel_hi:[1,0]
	v_pk_add_f32 v[16:17], v[16:17], v[78:79] op_sel_hi:[1,0]
	v_pk_fma_f32 v[14:15], v[68:69], v[76:77], v[14:15] op_sel:[0,1,0] op_sel_hi:[1,1,1]
	v_pk_fma_f32 v[16:17], v[70:71], v[76:77], v[16:17] op_sel:[0,1,0] op_sel_hi:[1,1,1]
	v_pk_add_f32 v[34:35], v[34:35], v[14:15]
	v_pk_fma_f32 v[36:37], v[14:15], v[14:15], v[36:37]
	v_pk_add_f32 v[34:35], v[34:35], v[16:17]
	v_pk_fma_f32 v[36:37], v[16:17], v[16:17], v[36:37]
	s_waitcnt lgkmcnt(0)
	v_pk_add_f32 v[18:19], v[18:19], v[58:59]
	v_pk_add_f32 v[20:21], v[20:21], v[60:61]
	v_pk_add_f32 v[18:19], v[18:19], v[78:79] op_sel_hi:[1,0]
	v_pk_add_f32 v[20:21], v[20:21], v[78:79] op_sel_hi:[1,0]
	v_pk_fma_f32 v[18:19], v[72:73], v[76:77], v[18:19] op_sel:[0,1,0] op_sel_hi:[1,1,1]
	v_pk_fma_f32 v[20:21], v[74:75], v[76:77], v[20:21] op_sel:[0,1,0] op_sel_hi:[1,1,1]
	v_pk_add_f32 v[34:35], v[34:35], v[18:19]
	v_pk_fma_f32 v[36:37], v[18:19], v[18:19], v[36:37]
	v_pk_add_f32 v[34:35], v[34:35], v[20:21]
	v_pk_fma_f32 v[36:37], v[20:21], v[20:21], v[36:37]
	ds_read2st64_b32 v[50:51], v221 offset0:36 offset1:37
	ds_read2st64_b32 v[52:53], v221 offset0:38 offset1:39
	ds_read2st64_b32 v[62:63], v67 offset0:144 offset1:146
	ds_read2st64_b32 v[64:65], v67 offset0:148 offset1:150
	s_waitcnt lgkmcnt(0)
	v_pk_add_f32 v[22:23], v[22:23], v[50:51]
	v_pk_add_f32 v[24:25], v[24:25], v[52:53]
	v_pk_add_f32 v[22:23], v[22:23], v[78:79] op_sel_hi:[1,0]
	v_pk_add_f32 v[24:25], v[24:25], v[78:79] op_sel_hi:[1,0]
	v_pk_fma_f32 v[22:23], v[62:63], v[76:77], v[22:23] op_sel:[0,1,0] op_sel_hi:[1,1,1]
	v_pk_fma_f32 v[24:25], v[64:65], v[76:77], v[24:25] op_sel:[0,1,0] op_sel_hi:[1,1,1]
	v_pk_add_f32 v[34:35], v[34:35], v[22:23]
	v_pk_fma_f32 v[36:37], v[22:23], v[22:23], v[36:37]
	v_pk_add_f32 v[34:35], v[34:35], v[24:25]
	v_pk_fma_f32 v[36:37], v[24:25], v[24:25], v[36:37]
	s_mov_b64 s[40:41], exec
	s_and_b64 exec, exec, s[0:1]
	ds_read2st64_b32 v[50:51], v221 offset0:40 offset1:41
	ds_read2st64_b32 v[52:53], v221 offset0:42 offset1:43
	ds_read2st64_b32 v[62:63], v67 offset0:160 offset1:162
	ds_read2st64_b32 v[64:65], v67 offset0:164 offset1:166
	s_waitcnt lgkmcnt(0)
	v_pk_add_f32 v[26:27], v[26:27], v[50:51]
	v_pk_add_f32 v[28:29], v[28:29], v[52:53]
	v_pk_add_f32 v[26:27], v[26:27], v[78:79] op_sel_hi:[1,0]
	v_pk_add_f32 v[28:29], v[28:29], v[78:79] op_sel_hi:[1,0]
	v_pk_fma_f32 v[26:27], v[62:63], v[76:77], v[26:27] op_sel:[0,1,0] op_sel_hi:[1,1,1]
	v_pk_fma_f32 v[28:29], v[64:65], v[76:77], v[28:29] op_sel:[0,1,0] op_sel_hi:[1,1,1]
	v_pk_add_f32 v[34:35], v[34:35], v[26:27]
	v_pk_fma_f32 v[36:37], v[26:27], v[26:27], v[36:37]
	v_pk_add_f32 v[34:35], v[34:35], v[28:29]
	v_pk_fma_f32 v[36:37], v[28:29], v[28:29], v[36:37]
	s_mov_b64 exec, s[40:41]
	v_add_f32_e32 v34, v34, v35
	v_add_f32_e32 v36, v36, v37
	s_nop 1
	v_permlane32_swap_b32_e32 v34, v36
	v_add_f32_e32 v38, v34, v36
	ds_write_b32 v236, v38
